# phase 8 unit setup: both row blocks' token-index gathers in flight together (first gather's wait moved behind the second lookup)
# speedup vs baseline: 1.0163x; 1.0025x over previous
.LBB0_1007:
	s_ashr_i32 s10, s46, 31
	s_lshr_b32 s10, s10, 29
	s_add_i32 s10, s46, s10
	s_ashr_i32 s36, s10, 3
	s_mov_b64 s[98:99], exec
	s_mov_b64 exec, -1
	v_and_b32_e32 v2, 63, v250
	v_lshlrev_b32_e32 v2, 2, v2
	v_add_u32_e32 v2, 0x20000, v2
	ds_read_b32 v2, v2
	s_waitcnt lgkmcnt(0)
	v_cmp_ge_i32_e64 s[100:101], s36, v2
	s_bcnt1_i32_b64 s10, s[100:101]
	s_add_i32 s10, s10, -1
	s_mov_b64 exec, s[98:99]
	s_lshl_b32 s34, s10, 2
	s_add_i32 s34, s34, 0
	s_add_i32 s34, s34, 0x20000
	v_mov_b32_e32 v2, s34
	ds_read2_b32 v[4:5], v2 offset1:80
	ds_read_b32 v2, v2 offset:640
	s_mul_i32 s34, s10, 0x44
	s_add_i32 s48, s34, 0
	s_lshl_b32 s47, s10, 13
	s_waitcnt lgkmcnt(1)
	v_readfirstlane_b32 s35, v4
	s_sub_i32 s35, s36, s35
	v_readfirstlane_b32 s37, v5
	s_lshl_b32 s49, s35, 9
	s_sub_i32 s35, s37, s49
	s_min_i32 s50, s35, 0x200
	s_add_i32 s48, s48, 0x20400
	v_cmp_gt_i32_e32 vcc, s50, v0
	v_mov_b32_e32 v136, 0
	v_mov_b32_e32 v3, 0
	s_and_saveexec_b64 s[34:35], vcc
	s_cbranch_execz .LBB0_1011
	v_mov_b32_e32 v3, s48
	ds_read_b32 v3, v3 offset:32
	v_add_u32_e32 v4, s49, v0
	s_waitcnt lgkmcnt(0)
	v_cmp_gt_i32_e32 vcc, v3, v4
	s_nop 1
	v_cndmask_b32_e64 v3, 8, 0, vcc
	v_lshl_add_u32 v5, v3, 2, s48
	ds_read_b32 v5, v5 offset:16
	v_or_b32_e32 v6, 4, v3
	s_waitcnt lgkmcnt(0)
	v_cmp_gt_i32_e32 vcc, v5, v4
	s_nop 1
	v_cndmask_b32_e32 v3, v6, v3, vcc
	v_lshl_add_u32 v5, v3, 2, s48
	ds_read_b32 v5, v5 offset:8
	v_or_b32_e32 v6, 2, v3
	s_waitcnt lgkmcnt(0)
	v_cmp_gt_i32_e32 vcc, v5, v4
	s_nop 1
	v_cndmask_b32_e32 v3, v6, v3, vcc
	v_lshl_add_u32 v5, v3, 2, s48
	ds_read_b32 v5, v5 offset:4
	v_or_b32_e32 v6, 1, v3
	s_waitcnt lgkmcnt(0)
	v_cmp_gt_i32_e32 vcc, v5, v4
	s_nop 1
	v_cndmask_b32_e32 v3, v6, v3, vcc
	v_lshl_add_u32 v5, v3, 2, s48
	ds_read_b32 v5, v5
	v_add_u32_e32 v4, s47, v4
	s_waitcnt lgkmcnt(0)
	v_sub_u32_e32 v4, v4, v5
	v_lshl_add_u32 v4, v3, 9, v4
	v_ashrrev_i32_e32 v5, 31, v4
	v_lshl_add_u64 v[4:5], v[4:5], 2, s[6:7]
	global_load_dword v3, v[4:5], off
.LBB0_1011:
	s_or_b64 exec, exec, s[34:35]
	v_cmp_gt_i32_e32 vcc, s50, v167
	s_and_saveexec_b64 s[34:35], vcc
	s_cbranch_execz .LBB0_1013
	v_mov_b32_e32 v4, s48
	ds_read_b32 v4, v4 offset:32
	v_add_u32_e32 v5, s49, v167
	s_waitcnt lgkmcnt(0)
	v_cmp_gt_i32_e32 vcc, v4, v5
	s_nop 1
	v_cndmask_b32_e64 v4, 8, 0, vcc
	v_lshl_add_u32 v6, v4, 2, s48
	ds_read_b32 v6, v6 offset:16
	v_or_b32_e32 v7, 4, v4
	s_waitcnt lgkmcnt(0)
	v_cmp_gt_i32_e32 vcc, v6, v5
	s_nop 1
	v_cndmask_b32_e32 v4, v7, v4, vcc
	v_lshl_add_u32 v6, v4, 2, s48
	ds_read_b32 v6, v6 offset:8
	v_or_b32_e32 v7, 2, v4
	s_waitcnt lgkmcnt(0)
	v_cmp_gt_i32_e32 vcc, v6, v5
	s_nop 1
	v_cndmask_b32_e32 v4, v7, v4, vcc
	v_lshl_add_u32 v6, v4, 2, s48
	ds_read_b32 v6, v6 offset:4
	v_or_b32_e32 v7, 1, v4
	s_waitcnt lgkmcnt(0)
	v_cmp_gt_i32_e32 vcc, v6, v5
	s_nop 1
	v_cndmask_b32_e32 v4, v7, v4, vcc
	v_lshl_add_u32 v6, v4, 2, s48
	ds_read_b32 v6, v6
	v_add_u32_e32 v5, s47, v5
	s_waitcnt lgkmcnt(0)
	v_sub_u32_e32 v5, v5, v6
	v_lshl_add_u32 v4, v4, 9, v5
	v_ashrrev_i32_e32 v5, 31, v4
	v_lshl_add_u64 v[4:5], v[4:5], 2, s[6:7]
	global_load_dword v4, v[4:5], off
	s_waitcnt vmcnt(0)
	v_lshlrev_b32_e32 v4, 11, v4
	v_and_b32_e32 v136, 0x7fff800, v4
.LBB0_1013:
	s_or_b64 exec, exec, s[34:35]
	s_waitcnt vmcnt(0)
	v_lshlrev_b32_e32 v3, 11, v3
	v_and_b32_e32 v3, 0x7fff800, v3
	s_lshl_b64 s[34:35], s[10:11], 22
	s_add_u32 s10, s12, s34
	s_addc_u32 s52, s13, s35
	s_lshl_b32 s34, s36, 9
	s_lshl_b32 s35, s46, 6
	s_sub_i32 s34, s35, s34
	s_ashr_i32 s35, s34, 31
	s_lshl_b64 s[36:37], s[34:35], 2
	s_add_u32 s36, s10, s36
	s_addc_u32 s37, s52, s37
	v_or_b32_e32 v146, v3, v1
	s_waitcnt lgkmcnt(0)
	v_readfirstlane_b32 s51, v2
	v_lshl_add_u64 v[2:3], s[36:37], 0, v[152:153]
	v_lshl_add_u64 v[156:157], v[2:3], 0, v[148:149]
	s_mov_b64 s[36:37], -1
	s_cmp_ge_i32 s38, s50
	v_lshl_add_u64 v[132:133], v[156:157], 0, s[22:23]
	v_lshl_add_u64 v[130:131], v[156:157], 0, s[24:25]
	v_lshl_add_u64 v[134:135], v[156:157], 0, s[26:27]
	v_lshl_add_u64 v[138:139], v[156:157], 0, s[28:29]
	v_lshl_add_u64 v[142:143], v[156:157], 0, s[30:31]
	s_cbranch_scc0 .LBB0_1017
	global_load_dwordx4 v[2:5], v[156:157], off sc1 nt
	s_mov_b32 m0, s39
	global_load_dwordx4 v[6:9], v[132:133], off sc1 nt
	v_lshl_add_u64 v[50:51], s[14:15], 0, v[146:147]
	global_load_lds_dwordx4 v146, s[14:15]
	global_load_dwordx4 v[34:37], v[130:131], off sc1 nt
	global_load_dwordx4 v[38:41], v[134:135], off sc1 nt
	s_mov_b32 m0, s40
	s_nop 0
	global_load_lds_dwordx4 v146, s[16:17]
	s_waitcnt vmcnt(4)
	s_nop 0
	v_cvt_pk_bf16_f32 v2, v2, v6
	ds_write_b32 v169, v2 offset:49152
	v_cvt_pk_bf16_f32 v2, v3, v7
	ds_write_b32 v169, v2 offset:49216
	v_cvt_pk_bf16_f32 v2, v4, v8
	ds_write_b32 v169, v2 offset:49280
	v_cvt_pk_bf16_f32 v2, v5, v9
	ds_write_b32 v169, v2 offset:49344
	global_load_dwordx4 v[42:45], v[138:139], off sc1 nt
	global_load_dwordx4 v[46:49], v[142:143], off sc1 nt
	s_waitcnt vmcnt(5)
	s_mov_b32 m0, s41
	s_waitcnt lgkmcnt(0)
	s_barrier
	global_load_lds_dwordx4 v146, s[18:19]
	v_mov_b32_e32 v2, 0
	s_mov_b32 s37, -2
	s_movk_i32 s36, 0x80
	v_mov_b32_e32 v3, v2
	v_mov_b32_e32 v4, v2
	v_mov_b32_e32 v5, v2
	v_mov_b32_e32 v6, v2
	v_mov_b32_e32 v7, v2
	v_mov_b32_e32 v8, v2
	v_mov_b32_e32 v9, v2
	v_mov_b32_e32 v10, v2
	v_mov_b32_e32 v11, v2
	v_mov_b32_e32 v12, v2
	v_mov_b32_e32 v13, v2
	v_mov_b32_e32 v14, v2
	v_mov_b32_e32 v15, v2
	v_mov_b32_e32 v16, v2
	v_mov_b32_e32 v17, v2
	v_mov_b32_e32 v66, v2
	v_mov_b32_e32 v67, v2
	v_mov_b32_e32 v68, v2
	v_mov_b32_e32 v69, v2
	v_mov_b32_e32 v70, v2
	v_mov_b32_e32 v71, v2
	v_mov_b32_e32 v72, v2
	v_mov_b32_e32 v73, v2
	v_mov_b32_e32 v74, v2
	v_mov_b32_e32 v75, v2
	v_mov_b32_e32 v76, v2
	v_mov_b32_e32 v77, v2
	v_mov_b32_e32 v78, v2
	v_mov_b32_e32 v79, v2
	v_mov_b32_e32 v80, v2
	v_mov_b32_e32 v81, v2
	v_mov_b32_e32 v18, v2
	v_mov_b32_e32 v19, v2
	v_mov_b32_e32 v20, v2
	v_mov_b32_e32 v21, v2
	v_mov_b32_e32 v22, v2
	v_mov_b32_e32 v23, v2
	v_mov_b32_e32 v24, v2
	v_mov_b32_e32 v25, v2
	v_mov_b32_e32 v26, v2
	v_mov_b32_e32 v27, v2
	v_mov_b32_e32 v28, v2
	v_mov_b32_e32 v29, v2
	v_mov_b32_e32 v30, v2
	v_mov_b32_e32 v31, v2
	v_mov_b32_e32 v32, v2
	v_mov_b32_e32 v33, v2
	v_mov_b32_e32 v114, v2
	v_mov_b32_e32 v115, v2
	v_mov_b32_e32 v116, v2
	v_mov_b32_e32 v117, v2
	v_mov_b32_e32 v118, v2
	v_mov_b32_e32 v119, v2
	v_mov_b32_e32 v120, v2
	v_mov_b32_e32 v121, v2
	v_mov_b32_e32 v122, v2
	v_mov_b32_e32 v123, v2
	v_mov_b32_e32 v124, v2
	v_mov_b32_e32 v125, v2
	v_mov_b32_e32 v126, v2
	v_mov_b32_e32 v127, v2
	v_mov_b32_e32 v128, v2
	v_mov_b32_e32 v129, v2
	v_readfirstlane_b32 s98, v250
	s_bitcmp1_b32 s98, 6
	s_cbranch_scc1 .Lmoe_B_1015
